# convpre LayerNorm wave reductions via DPP/permlane swaps instead of ds_bpermute chains (latency-bound phase); skew0; flat barrier
# speedup vs baseline: 1.0001x; 1.0001x over previous
; __device__ __forceinline__ unsigned pk2(float lo, float hi) { f32x2_m v = {lo, hi}; bf16x2_m b = __builtin_convertvector(v, bf16x2_m); return __builtin_bit_cast(unsigned, b); }
; __device__ __forceinline__ float sigmoid_f(float x) { return __builtin_amdgcn_rcpf(1.0f + __builtin_amdgcn_exp2f(-LOG2E * x)); }
; __device__ __forceinline__ float wave_sum(float v) {
; #pragma unroll
;     for (int o = 1; o < 64; o <<= 1) v += __shfl_xor(v, o);
;     return v;
; }
; __device__ __forceinline__ void convpre_phase(const Ctx& C, const bf16* Z, const float* dw_w, const float* dw_b, const float* ln_g, const float* ln_b, bf16* ZC) {
;     ...
;             for (int q = 0; q < 4; ++q) {
;                 float s = 0.f;
; #pragma unroll
;                 for (int i = 0; i < 8; ++i) s += acc[q][i];
;                 const float mean = wave_sum(s) * (1.0f / CONV_CH); float s2 = 0.f;
; #pragma unroll
;                 for (int i = 0; i < 8; ++i) { acc[q][i] -= mean; s2 += acc[q][i] * acc[q][i]; }
;                 const float rstd = 1.0f / sqrtf(wave_sum(s2) * (1.0f / CONV_CH) + LN_EPS);
;                 float y[8];
; #pragma unroll
;                 for (int i = 0; i < 8; ++i) { const float u = acc[q][i] * rstd * lg[i] + lb[i]; y[i] = u * sigmoid_f(u); }
;                 v4u o; o.x = pk2(y[0], y[1]); o.y = pk2(y[2], y[3]); o.z = pk2(y[4], y[5]); o.w = pk2(y[6], y[7]);
;                 __builtin_amdgcn_raw_buffer_store_b128(o, zrs, (int)(((size_t)(t0 + tt + q) * CONV_CH + c0) * 2), 0, 16); }
.LBB0_477:
	v_add_f32_e32 v60, 0, v52
	v_add_f32_e32 v60, v53, v60
	v_add_f32_e32 v60, v54, v60
	v_add_f32_e32 v60, v55, v60
	v_add_f32_e32 v60, v56, v60
	v_add_f32_e32 v60, v57, v60
	v_add_f32_e32 v60, v58, v60
	v_add_f32_e32 v60, v59, v60
	s_nop 1
	v_mov_b32_dpp v61, v60 quad_perm:[1,0,3,2] row_mask:0xf bank_mask:0xf
	s_mov_b32 s22, 0xf800000
	v_readlane_b32 s0, v253, 58
	s_add_i32 s21, s21, s0
	v_readlane_b32 s24, v254, 3
	s_waitcnt lgkmcnt(0)
	v_add_f32_e32 v60, v60, v61
	s_nop 1
	v_mov_b32_dpp v61, v60 quad_perm:[2,3,0,1] row_mask:0xf bank_mask:0xf
	v_readlane_b32 s25, v254, 4
	v_readlane_b32 s26, v254, 5
	v_readlane_b32 s27, v254, 6
	s_waitcnt lgkmcnt(0)
	v_add_f32_e32 v60, v60, v61
	s_nop 1
	v_mov_b32_dpp v61, v60 row_half_mirror row_mask:0xf bank_mask:0xf
	s_waitcnt lgkmcnt(0)
	v_add_f32_e32 v60, v60, v61
	s_nop 1
	v_mov_b32_dpp v61, v60 row_mirror row_mask:0xf bank_mask:0xf
	s_waitcnt lgkmcnt(0)
	v_add_f32_e32 v60, v60, v61
	v_mov_b32_e32 v61, v60
	s_nop 1
	v_permlane16_swap_b32_e32 v60, v61
	s_waitcnt lgkmcnt(0)
	v_add_f32_e32 v60, v60, v61
	v_mov_b32_e32 v61, v60
	s_nop 1
	v_permlane32_swap_b32_e32 v60, v61
	s_waitcnt lgkmcnt(0)
	v_add_f32_e32 v60, v60, v61
	v_mul_f32_e32 v60, 0x3b000000, v60
	v_pk_add_f32 v[52:53], v[52:53], v[60:61] op_sel_hi:[1,0] neg_lo:[0,1] neg_hi:[0,1]
	v_pk_add_f32 v[58:59], v[58:59], v[60:61] op_sel_hi:[1,0] neg_lo:[0,1] neg_hi:[0,1]
	v_pk_add_f32 v[56:57], v[56:57], v[60:61] op_sel_hi:[1,0] neg_lo:[0,1] neg_hi:[0,1]
	v_pk_add_f32 v[54:55], v[54:55], v[60:61] op_sel_hi:[1,0] neg_lo:[0,1] neg_hi:[0,1]
	v_pk_mul_f32 v[60:61], v[52:53], v[52:53]
	v_pk_mul_f32 v[66:67], v[54:55], v[54:55]
	v_add_f32_e32 v60, v60, v61
	v_add_f32_e32 v60, v66, v60
	v_pk_mul_f32 v[64:65], v[56:57], v[56:57]
	v_add_f32_e32 v60, v67, v60
	v_add_f32_e32 v60, v64, v60
	v_pk_mul_f32 v[62:63], v[58:59], v[58:59]
	v_add_f32_e32 v60, v65, v60
	v_add_f32_e32 v60, v62, v60
	v_add_f32_e32 v60, v63, v60
	s_nop 1
	v_mov_b32_dpp v61, v60 quad_perm:[1,0,3,2] row_mask:0xf bank_mask:0xf
	s_waitcnt lgkmcnt(0)
	v_add_f32_e32 v60, v60, v61
	s_nop 1
	v_mov_b32_dpp v61, v60 quad_perm:[2,3,0,1] row_mask:0xf bank_mask:0xf
	s_waitcnt lgkmcnt(0)
	v_add_f32_e32 v60, v60, v61
	s_nop 1
	v_mov_b32_dpp v61, v60 row_half_mirror row_mask:0xf bank_mask:0xf
	s_waitcnt lgkmcnt(0)
	v_add_f32_e32 v60, v60, v61
	s_nop 1
	v_mov_b32_dpp v61, v60 row_mirror row_mask:0xf bank_mask:0xf
	s_waitcnt lgkmcnt(0)
	v_add_f32_e32 v60, v60, v61
	v_mov_b32_e32 v61, v60
	s_nop 1
	v_permlane16_swap_b32_e32 v60, v61
	s_waitcnt lgkmcnt(0)
	v_add_f32_e32 v60, v60, v61
	v_mov_b32_e32 v61, v60
	s_nop 1
	v_permlane32_swap_b32_e32 v60, v61
	s_waitcnt lgkmcnt(0)
	v_add_f32_e32 v60, v60, v61
	v_fmamk_f32 v60, v60, 0x3b000000, v210
	v_cmp_gt_f32_e32 vcc, s22, v60
	v_mul_f32_e32 v61, 0x4f800000, v60
	s_nop 0
	v_cndmask_b32_e32 v60, v60, v61, vcc
	v_sqrt_f32_e32 v61, v60
	s_nop 0
	v_add_u32_e32 v62, -1, v61
	v_fma_f32 v63, -v62, v61, v60
	v_cmp_ge_f32_e64 s[18:19], 0, v63
	v_add_u32_e32 v63, 1, v61
	s_nop 0
	v_cndmask_b32_e64 v62, v61, v62, s[18:19]
	v_fma_f32 v61, -v63, v61, v60
	v_cmp_lt_f32_e64 s[18:19], 0, v61
	s_nop 1
	v_cndmask_b32_e64 v61, v62, v63, s[18:19]
	v_mul_f32_e32 v62, 0x37800000, v61
	v_cndmask_b32_e32 v61, v61, v62, vcc
	v_cmp_class_f32_e32 vcc, v60, v211
	s_nop 1
	v_cndmask_b32_e32 v60, v61, v60, vcc
	v_div_scale_f32 v61, s[0:1], v60, v60, 1.0
	v_rcp_f32_e32 v62, v61
	s_lshl_b32 s0, s21, 10
	v_fma_f32 v63, -v61, v62, 1.0
	v_fmac_f32_e32 v62, v63, v62
	v_div_scale_f32 v63, vcc, 1.0, v60, 1.0
	v_mul_f32_e32 v64, v63, v62
	v_fma_f32 v65, -v61, v64, v63
	v_fmac_f32_e32 v64, v65, v62
	v_fma_f32 v61, -v61, v64, v63
	v_div_fmas_f32 v61, v61, v62, v64
	v_div_fixup_f32 v60, v61, v60, 1.0
	v_pk_mul_f32 v[52:53], v[52:53], v[60:61] op_sel_hi:[1,0]
	s_waitcnt vmcnt(0)
	v_pk_fma_f32 v[52:53], v[16:17], v[52:53], v[24:25]
	s_nop 0
	v_mul_f32_e32 v61, 0xbfb8aa3b, v52
	v_exp_f32_e32 v61, v61
	s_nop 0
	v_add_f32_e32 v61, 1.0, v61
	v_rcp_f32_e32 v62, v61
	v_mul_f32_e32 v61, 0xbfb8aa3b, v53
	v_exp_f32_e32 v61, v61
	s_nop 0
	v_add_f32_e32 v61, 1.0, v61
	v_pk_mul_f32 v[54:55], v[54:55], v[60:61] op_sel_hi:[1,0]
	v_rcp_f32_e32 v63, v61
	v_pk_fma_f32 v[54:55], v[18:19], v[54:55], v[26:27]
	v_pk_mul_f32 v[52:53], v[52:53], v[62:63]
	v_mul_f32_e32 v61, 0xbfb8aa3b, v54
	v_exp_f32_e32 v61, v61
	v_cvt_pk_bf16_f32 v52, v52, v53
	v_add_f32_e32 v61, 1.0, v61
	v_rcp_f32_e32 v62, v61
	v_mul_f32_e32 v61, 0xbfb8aa3b, v55
	v_exp_f32_e32 v61, v61
	s_nop 0
	v_add_f32_e32 v61, 1.0, v61
	v_pk_mul_f32 v[56:57], v[56:57], v[60:61] op_sel_hi:[1,0]
	v_rcp_f32_e32 v63, v61
	v_pk_fma_f32 v[56:57], v[12:13], v[56:57], v[20:21]
	v_pk_mul_f32 v[54:55], v[54:55], v[62:63]
	v_mul_f32_e32 v61, 0xbfb8aa3b, v56
	v_exp_f32_e32 v61, v61
	v_cvt_pk_bf16_f32 v53, v54, v55
	v_add_f32_e32 v61, 1.0, v61
	v_rcp_f32_e32 v62, v61
	v_mul_f32_e32 v61, 0xbfb8aa3b, v57
	v_exp_f32_e32 v61, v61
	s_nop 0
	v_add_f32_e32 v61, 1.0, v61
	v_pk_mul_f32 v[58:59], v[58:59], v[60:61] op_sel_hi:[1,0]
	v_rcp_f32_e32 v63, v61
	v_pk_fma_f32 v[58:59], v[14:15], v[58:59], v[22:23]
	v_pk_mul_f32 v[56:57], v[56:57], v[62:63]
	v_mul_f32_e32 v60, 0xbfb8aa3b, v58
	v_mul_f32_e32 v61, 0xbfb8aa3b, v59
	v_exp_f32_e32 v60, v60
	v_exp_f32_e32 v61, v61
	v_cvt_pk_bf16_f32 v54, v56, v57
	v_add_u32_e32 v56, s0, v3
	v_add_f32_e32 v60, 1.0, v60
	v_add_f32_e32 v61, 1.0, v61
	v_rcp_f32_e32 v60, v60
	v_rcp_f32_e32 v61, v61
	s_nop 0
	v_pk_mul_f32 v[58:59], v[58:59], v[60:61]
	s_nop 0
	v_cvt_pk_bf16_f32 v55, v58, v59
	buffer_store_dwordx4 v[52:55], v56, s[24:27], 0 offen sc1
	s_nop 1
	v_add_f32_e32 v52, 0, v44
	v_add_f32_e32 v52, v45, v52
	v_add_f32_e32 v52, v46, v52
	v_add_f32_e32 v52, v47, v52
	v_add_f32_e32 v52, v48, v52
	v_add_f32_e32 v52, v49, v52
	v_add_f32_e32 v52, v50, v52
	v_add_f32_e32 v52, v51, v52
	s_nop 1
	v_mov_b32_dpp v53, v52 quad_perm:[1,0,3,2] row_mask:0xf bank_mask:0xf
	s_waitcnt lgkmcnt(0)
; __device__ __forceinline__ unsigned pk2(float lo, float hi) { f32x2_m v = {lo, hi}; bf16x2_m b = __builtin_convertvector(v, bf16x2_m); return __builtin_bit_cast(unsigned, b); }
; __device__ __forceinline__ float sigmoid_f(float x) { return __builtin_amdgcn_rcpf(1.0f + __builtin_amdgcn_exp2f(-LOG2E * x)); }
; __device__ __forceinline__ float wave_sum(float v) {
; #pragma unroll
;     for (int o = 1; o < 64; o <<= 1) v += __shfl_xor(v, o);
;     return v;
; }
; __device__ __forceinline__ void convpre_phase(const Ctx& C, const bf16* Z, const float* dw_w, const float* dw_b, const float* ln_g, const float* ln_b, bf16* ZC) {
;     ...
;             for (int q = 0; q < 4; ++q) {
;                 float s = 0.f;
; #pragma unroll
;                 for (int i = 0; i < 8; ++i) s += acc[q][i];
;                 const float mean = wave_sum(s) * (1.0f / CONV_CH); float s2 = 0.f;
; #pragma unroll
;                 for (int i = 0; i < 8; ++i) { acc[q][i] -= mean; s2 += acc[q][i] * acc[q][i]; }
;                 const float rstd = 1.0f / sqrtf(wave_sum(s2) * (1.0f / CONV_CH) + LN_EPS);
;                 float y[8];
; #pragma unroll
;                 for (int i = 0; i < 8; ++i) { const float u = acc[q][i] * rstd * lg[i] + lb[i]; y[i] = u * sigmoid_f(u); }
;                 v4u o; o.x = pk2(y[0], y[1]); o.y = pk2(y[2], y[3]); o.z = pk2(y[4], y[5]); o.w = pk2(y[6], y[7]);
;                 __builtin_amdgcn_raw_buffer_store_b128(o, zrs, (int)(((size_t)(t0 + tt + q) * CONV_CH + c0) * 2), 0, 16); }
	v_add_f32_e32 v52, v52, v53
	s_nop 1
	v_mov_b32_dpp v53, v52 quad_perm:[2,3,0,1] row_mask:0xf bank_mask:0xf
	s_waitcnt lgkmcnt(0)
	v_add_f32_e32 v52, v52, v53
	s_nop 1
	v_mov_b32_dpp v53, v52 row_half_mirror row_mask:0xf bank_mask:0xf
	s_waitcnt lgkmcnt(0)
	v_add_f32_e32 v52, v52, v53
	s_nop 1
	v_mov_b32_dpp v53, v52 row_mirror row_mask:0xf bank_mask:0xf
	s_waitcnt lgkmcnt(0)
	v_add_f32_e32 v52, v52, v53
	v_mov_b32_e32 v53, v52
	s_nop 1
	v_permlane16_swap_b32_e32 v52, v53
	s_waitcnt lgkmcnt(0)
	v_add_f32_e32 v52, v52, v53
	v_mov_b32_e32 v53, v52
	s_nop 1
	v_permlane32_swap_b32_e32 v52, v53
	s_waitcnt lgkmcnt(0)
	v_add_f32_e32 v52, v52, v53
	v_mul_f32_e32 v52, 0x3b000000, v52
	v_pk_add_f32 v[44:45], v[44:45], v[52:53] op_sel_hi:[1,0] neg_lo:[0,1] neg_hi:[0,1]
	v_pk_add_f32 v[50:51], v[50:51], v[52:53] op_sel_hi:[1,0] neg_lo:[0,1] neg_hi:[0,1]
	v_pk_add_f32 v[48:49], v[48:49], v[52:53] op_sel_hi:[1,0] neg_lo:[0,1] neg_hi:[0,1]
	v_pk_add_f32 v[46:47], v[46:47], v[52:53] op_sel_hi:[1,0] neg_lo:[0,1] neg_hi:[0,1]
	v_pk_mul_f32 v[52:53], v[44:45], v[44:45]
	v_pk_mul_f32 v[58:59], v[46:47], v[46:47]
	v_add_f32_e32 v52, v52, v53
	v_add_f32_e32 v52, v58, v52
	v_pk_mul_f32 v[56:57], v[48:49], v[48:49]
	v_add_f32_e32 v52, v59, v52
	v_add_f32_e32 v52, v56, v52
	v_pk_mul_f32 v[54:55], v[50:51], v[50:51]
	v_add_f32_e32 v52, v57, v52
	v_add_f32_e32 v52, v54, v52
	v_add_f32_e32 v52, v55, v52
	s_nop 1
	v_mov_b32_dpp v53, v52 quad_perm:[1,0,3,2] row_mask:0xf bank_mask:0xf
	s_waitcnt lgkmcnt(0)
	v_add_f32_e32 v52, v52, v53
	s_nop 1
	v_mov_b32_dpp v53, v52 quad_perm:[2,3,0,1] row_mask:0xf bank_mask:0xf
	s_waitcnt lgkmcnt(0)
	v_add_f32_e32 v52, v52, v53
	s_nop 1
	v_mov_b32_dpp v53, v52 row_half_mirror row_mask:0xf bank_mask:0xf
	s_waitcnt lgkmcnt(0)
	v_add_f32_e32 v52, v52, v53
	s_nop 1
	v_mov_b32_dpp v53, v52 row_mirror row_mask:0xf bank_mask:0xf
	s_waitcnt lgkmcnt(0)
	v_add_f32_e32 v52, v52, v53
	v_mov_b32_e32 v53, v52
	s_nop 1
	v_permlane16_swap_b32_e32 v52, v53
	s_waitcnt lgkmcnt(0)
	v_add_f32_e32 v52, v52, v53
	v_mov_b32_e32 v53, v52
	s_nop 1
	v_permlane32_swap_b32_e32 v52, v53
	s_waitcnt lgkmcnt(0)
	v_add_f32_e32 v52, v52, v53
	v_fmamk_f32 v52, v52, 0x3b000000, v210
	v_cmp_gt_f32_e32 vcc, s22, v52
	v_mul_f32_e32 v53, 0x4f800000, v52
	s_nop 0
	v_cndmask_b32_e32 v52, v52, v53, vcc
	v_sqrt_f32_e32 v53, v52
	s_nop 0
	v_add_u32_e32 v54, -1, v53
	v_fma_f32 v55, -v54, v53, v52
	v_cmp_ge_f32_e64 s[18:19], 0, v55
	v_add_u32_e32 v55, 1, v53
	s_nop 0
	v_cndmask_b32_e64 v54, v53, v54, s[18:19]
	v_fma_f32 v53, -v55, v53, v52
	v_cmp_lt_f32_e64 s[18:19], 0, v53
	s_nop 1
	v_cndmask_b32_e64 v53, v54, v55, s[18:19]
	v_mul_f32_e32 v54, 0x37800000, v53
	v_cndmask_b32_e32 v53, v53, v54, vcc
	v_cmp_class_f32_e32 vcc, v52, v211
	s_nop 1
	v_cndmask_b32_e32 v52, v53, v52, vcc
	v_div_scale_f32 v53, s[18:19], v52, v52, 1.0
	v_rcp_f32_e32 v54, v53
	s_nop 0
	v_fma_f32 v55, -v53, v54, 1.0
	v_fmac_f32_e32 v54, v55, v54
	v_div_scale_f32 v55, vcc, 1.0, v52, 1.0
	v_mul_f32_e32 v56, v55, v54
	v_fma_f32 v57, -v53, v56, v55
	v_fmac_f32_e32 v56, v57, v54
	v_fma_f32 v53, -v53, v56, v55
	v_div_fmas_f32 v53, v53, v54, v56
	v_div_fixup_f32 v52, v53, v52, 1.0
	v_pk_mul_f32 v[44:45], v[44:45], v[52:53] op_sel_hi:[1,0]
	s_nop 0
	v_pk_fma_f32 v[44:45], v[16:17], v[44:45], v[24:25]
	s_nop 0
	v_mul_f32_e32 v53, 0xbfb8aa3b, v44
	v_exp_f32_e32 v53, v53
	s_nop 0
	v_add_f32_e32 v53, 1.0, v53
	v_rcp_f32_e32 v54, v53
	v_mul_f32_e32 v53, 0xbfb8aa3b, v45
	v_exp_f32_e32 v53, v53
	s_nop 0
	v_add_f32_e32 v53, 1.0, v53
	v_pk_mul_f32 v[46:47], v[46:47], v[52:53] op_sel_hi:[1,0]
	v_rcp_f32_e32 v55, v53
	v_pk_fma_f32 v[46:47], v[18:19], v[46:47], v[26:27]
	v_pk_mul_f32 v[44:45], v[44:45], v[54:55]
	v_mul_f32_e32 v53, 0xbfb8aa3b, v46
	v_exp_f32_e32 v53, v53
	v_cvt_pk_bf16_f32 v44, v44, v45
	v_add_f32_e32 v53, 1.0, v53
	v_rcp_f32_e32 v54, v53
	v_mul_f32_e32 v53, 0xbfb8aa3b, v47
	v_exp_f32_e32 v53, v53
	s_nop 0
	v_add_f32_e32 v53, 1.0, v53
	v_pk_mul_f32 v[48:49], v[48:49], v[52:53] op_sel_hi:[1,0]
	v_rcp_f32_e32 v55, v53
	v_pk_fma_f32 v[48:49], v[12:13], v[48:49], v[20:21]
	v_pk_mul_f32 v[46:47], v[46:47], v[54:55]
	v_mul_f32_e32 v53, 0xbfb8aa3b, v48
	v_exp_f32_e32 v53, v53
	v_cvt_pk_bf16_f32 v45, v46, v47
	v_add_f32_e32 v53, 1.0, v53
	v_rcp_f32_e32 v54, v53
	v_mul_f32_e32 v53, 0xbfb8aa3b, v49
	v_exp_f32_e32 v53, v53
	s_nop 0
	v_add_f32_e32 v53, 1.0, v53
	v_pk_mul_f32 v[50:51], v[50:51], v[52:53] op_sel_hi:[1,0]
	v_rcp_f32_e32 v55, v53
	v_pk_fma_f32 v[50:51], v[14:15], v[50:51], v[22:23]
	v_pk_mul_f32 v[48:49], v[48:49], v[54:55]
	v_mul_f32_e32 v52, 0xbfb8aa3b, v50
	v_mul_f32_e32 v53, 0xbfb8aa3b, v51
	v_exp_f32_e32 v52, v52
	v_exp_f32_e32 v53, v53
	v_cvt_pk_bf16_f32 v46, v48, v49
	v_add_u32_e32 v48, s0, v106
	v_add_f32_e32 v52, 1.0, v52
	v_add_f32_e32 v53, 1.0, v53
	v_rcp_f32_e32 v52, v52
	v_rcp_f32_e32 v53, v53
	s_nop 0
	v_pk_mul_f32 v[50:51], v[50:51], v[52:53]
	s_nop 0
	v_cvt_pk_bf16_f32 v47, v50, v51
	buffer_store_dwordx4 v[44:47], v48, s[24:27], 0 offen sc1
	s_nop 1
	v_add_f32_e32 v44, 0, v36
	v_add_f32_e32 v44, v37, v44
	v_add_f32_e32 v44, v38, v44
	v_add_f32_e32 v44, v39, v44
	v_add_f32_e32 v44, v40, v44
	v_add_f32_e32 v44, v41, v44
	v_add_f32_e32 v44, v42, v44
	v_add_f32_e32 v44, v43, v44
	s_nop 1
	v_mov_b32_dpp v45, v44 quad_perm:[1,0,3,2] row_mask:0xf bank_mask:0xf
	s_waitcnt lgkmcnt(0)
	v_add_f32_e32 v44, v44, v45
	s_nop 1
	v_mov_b32_dpp v45, v44 quad_perm:[2,3,0,1] row_mask:0xf bank_mask:0xf
	s_waitcnt lgkmcnt(0)
	v_add_f32_e32 v44, v44, v45
	s_nop 1
	v_mov_b32_dpp v45, v44 row_half_mirror row_mask:0xf bank_mask:0xf
	s_waitcnt lgkmcnt(0)
	v_add_f32_e32 v44, v44, v45
	s_nop 1
	v_mov_b32_dpp v45, v44 row_mirror row_mask:0xf bank_mask:0xf
	s_waitcnt lgkmcnt(0)
; __device__ __forceinline__ unsigned pk2(float lo, float hi) { f32x2_m v = {lo, hi}; bf16x2_m b = __builtin_convertvector(v, bf16x2_m); return __builtin_bit_cast(unsigned, b); }
; __device__ __forceinline__ float sigmoid_f(float x) { return __builtin_amdgcn_rcpf(1.0f + __builtin_amdgcn_exp2f(-LOG2E * x)); }
; __device__ __forceinline__ float wave_sum(float v) {
; #pragma unroll
;     for (int o = 1; o < 64; o <<= 1) v += __shfl_xor(v, o);
;     return v;
; }
; __device__ __forceinline__ void convpre_phase(const Ctx& C, const bf16* Z, const float* dw_w, const float* dw_b, const float* ln_g, const float* ln_b, bf16* ZC) {
;     ...
;             for (int q = 0; q < 4; ++q) {
;                 float s = 0.f;
; #pragma unroll
;                 for (int i = 0; i < 8; ++i) s += acc[q][i];
;                 const float mean = wave_sum(s) * (1.0f / CONV_CH); float s2 = 0.f;
; #pragma unroll
;                 for (int i = 0; i < 8; ++i) { acc[q][i] -= mean; s2 += acc[q][i] * acc[q][i]; }
;                 const float rstd = 1.0f / sqrtf(wave_sum(s2) * (1.0f / CONV_CH) + LN_EPS);
;                 float y[8];
; #pragma unroll
;                 for (int i = 0; i < 8; ++i) { const float u = acc[q][i] * rstd * lg[i] + lb[i]; y[i] = u * sigmoid_f(u); }
;                 v4u o; o.x = pk2(y[0], y[1]); o.y = pk2(y[2], y[3]); o.z = pk2(y[4], y[5]); o.w = pk2(y[6], y[7]);
;                 __builtin_amdgcn_raw_buffer_store_b128(o, zrs, (int)(((size_t)(t0 + tt + q) * CONV_CH + c0) * 2), 0, 16); }
	v_add_f32_e32 v44, v44, v45
	v_mov_b32_e32 v45, v44
	s_nop 1
	v_permlane16_swap_b32_e32 v44, v45
	s_waitcnt lgkmcnt(0)
	v_add_f32_e32 v44, v44, v45
	v_mov_b32_e32 v45, v44
	s_nop 1
	v_permlane32_swap_b32_e32 v44, v45
	s_waitcnt lgkmcnt(0)
	v_add_f32_e32 v44, v44, v45
	v_mul_f32_e32 v44, 0x3b000000, v44
	v_pk_add_f32 v[36:37], v[36:37], v[44:45] op_sel_hi:[1,0] neg_lo:[0,1] neg_hi:[0,1]
	v_pk_add_f32 v[42:43], v[42:43], v[44:45] op_sel_hi:[1,0] neg_lo:[0,1] neg_hi:[0,1]
	v_pk_add_f32 v[40:41], v[40:41], v[44:45] op_sel_hi:[1,0] neg_lo:[0,1] neg_hi:[0,1]
	v_pk_add_f32 v[38:39], v[38:39], v[44:45] op_sel_hi:[1,0] neg_lo:[0,1] neg_hi:[0,1]
	v_pk_mul_f32 v[44:45], v[36:37], v[36:37]
	v_pk_mul_f32 v[50:51], v[38:39], v[38:39]
	v_add_f32_e32 v44, v44, v45
	v_add_f32_e32 v44, v50, v44
	v_pk_mul_f32 v[48:49], v[40:41], v[40:41]
	v_add_f32_e32 v44, v51, v44
	v_add_f32_e32 v44, v48, v44
	v_pk_mul_f32 v[46:47], v[42:43], v[42:43]
	v_add_f32_e32 v44, v49, v44
	v_add_f32_e32 v44, v46, v44
	v_add_f32_e32 v44, v47, v44
	s_nop 1
	v_mov_b32_dpp v45, v44 quad_perm:[1,0,3,2] row_mask:0xf bank_mask:0xf
	s_waitcnt lgkmcnt(0)
	v_add_f32_e32 v44, v44, v45
	s_nop 1
	v_mov_b32_dpp v45, v44 quad_perm:[2,3,0,1] row_mask:0xf bank_mask:0xf
	s_waitcnt lgkmcnt(0)
	v_add_f32_e32 v44, v44, v45
	s_nop 1
	v_mov_b32_dpp v45, v44 row_half_mirror row_mask:0xf bank_mask:0xf
	s_waitcnt lgkmcnt(0)
	v_add_f32_e32 v44, v44, v45
	s_nop 1
	v_mov_b32_dpp v45, v44 row_mirror row_mask:0xf bank_mask:0xf
	s_waitcnt lgkmcnt(0)
	v_add_f32_e32 v44, v44, v45
	v_mov_b32_e32 v45, v44
	s_nop 1
	v_permlane16_swap_b32_e32 v44, v45
	s_waitcnt lgkmcnt(0)
	v_add_f32_e32 v44, v44, v45
	v_mov_b32_e32 v45, v44
	s_nop 1
	v_permlane32_swap_b32_e32 v44, v45
	s_waitcnt lgkmcnt(0)
	v_add_f32_e32 v44, v44, v45
	v_fmamk_f32 v44, v44, 0x3b000000, v210
	v_cmp_gt_f32_e32 vcc, s22, v44
	v_mul_f32_e32 v45, 0x4f800000, v44
	s_nop 0
	v_cndmask_b32_e32 v44, v44, v45, vcc
	v_sqrt_f32_e32 v45, v44
	s_nop 0
	v_add_u32_e32 v46, -1, v45
	v_fma_f32 v47, -v46, v45, v44
	v_cmp_ge_f32_e64 s[18:19], 0, v47
	v_add_u32_e32 v47, 1, v45
	s_nop 0
	v_cndmask_b32_e64 v46, v45, v46, s[18:19]
	v_fma_f32 v45, -v47, v45, v44
	v_cmp_lt_f32_e64 s[18:19], 0, v45
	s_nop 1
	v_cndmask_b32_e64 v45, v46, v47, s[18:19]
	v_mul_f32_e32 v46, 0x37800000, v45
	v_cndmask_b32_e32 v45, v45, v46, vcc
	v_cmp_class_f32_e32 vcc, v44, v211
	s_nop 1
	v_cndmask_b32_e32 v44, v45, v44, vcc
	v_div_scale_f32 v45, s[18:19], v44, v44, 1.0
	v_rcp_f32_e32 v46, v45
	s_nop 0
	v_fma_f32 v47, -v45, v46, 1.0
	v_fmac_f32_e32 v46, v47, v46
	v_div_scale_f32 v47, vcc, 1.0, v44, 1.0
	v_mul_f32_e32 v48, v47, v46
	v_fma_f32 v49, -v45, v48, v47
	v_fmac_f32_e32 v48, v49, v46
	v_fma_f32 v45, -v45, v48, v47
	v_div_fmas_f32 v45, v45, v46, v48
	v_div_fixup_f32 v44, v45, v44, 1.0
	v_pk_mul_f32 v[36:37], v[36:37], v[44:45] op_sel_hi:[1,0]
	s_nop 0
	v_pk_fma_f32 v[36:37], v[16:17], v[36:37], v[24:25]
	s_nop 0
	v_mul_f32_e32 v45, 0xbfb8aa3b, v36
	v_exp_f32_e32 v45, v45
	s_nop 0
	v_add_f32_e32 v45, 1.0, v45
	v_rcp_f32_e32 v46, v45
	v_mul_f32_e32 v45, 0xbfb8aa3b, v37
	v_exp_f32_e32 v45, v45
	s_nop 0
	v_add_f32_e32 v45, 1.0, v45
	v_pk_mul_f32 v[38:39], v[38:39], v[44:45] op_sel_hi:[1,0]
	v_rcp_f32_e32 v47, v45
	v_pk_fma_f32 v[38:39], v[18:19], v[38:39], v[26:27]
	v_pk_mul_f32 v[36:37], v[36:37], v[46:47]
	v_mul_f32_e32 v45, 0xbfb8aa3b, v38
	v_exp_f32_e32 v45, v45
	v_cvt_pk_bf16_f32 v36, v36, v37
	v_add_f32_e32 v45, 1.0, v45
	v_rcp_f32_e32 v46, v45
	v_mul_f32_e32 v45, 0xbfb8aa3b, v39
	v_exp_f32_e32 v45, v45
	s_nop 0
	v_add_f32_e32 v45, 1.0, v45
	v_pk_mul_f32 v[40:41], v[40:41], v[44:45] op_sel_hi:[1,0]
	v_rcp_f32_e32 v47, v45
	v_pk_fma_f32 v[40:41], v[12:13], v[40:41], v[20:21]
	v_pk_mul_f32 v[38:39], v[38:39], v[46:47]
	v_mul_f32_e32 v45, 0xbfb8aa3b, v40
	v_exp_f32_e32 v45, v45
	v_cvt_pk_bf16_f32 v37, v38, v39
	v_add_f32_e32 v45, 1.0, v45
	v_rcp_f32_e32 v46, v45
	v_mul_f32_e32 v45, 0xbfb8aa3b, v41
	v_exp_f32_e32 v45, v45
	s_nop 0
	v_add_f32_e32 v45, 1.0, v45
	v_pk_mul_f32 v[42:43], v[42:43], v[44:45] op_sel_hi:[1,0]
	v_rcp_f32_e32 v47, v45
	v_pk_fma_f32 v[42:43], v[14:15], v[42:43], v[22:23]
	v_pk_mul_f32 v[40:41], v[40:41], v[46:47]
	v_mul_f32_e32 v44, 0xbfb8aa3b, v42
	v_mul_f32_e32 v45, 0xbfb8aa3b, v43
	v_exp_f32_e32 v44, v44
	v_exp_f32_e32 v45, v45
	v_cvt_pk_bf16_f32 v38, v40, v41
	v_add_u32_e32 v40, s0, v107
	v_add_f32_e32 v44, 1.0, v44
	v_add_f32_e32 v45, 1.0, v45
	v_rcp_f32_e32 v44, v44
	v_rcp_f32_e32 v45, v45
	s_nop 0
	v_pk_mul_f32 v[42:43], v[42:43], v[44:45]
	s_nop 0
	v_cvt_pk_bf16_f32 v39, v42, v43
	buffer_store_dwordx4 v[36:39], v40, s[24:27], 0 offen sc1
	s_nop 1
	v_add_f32_e32 v36, 0, v28
	v_add_f32_e32 v36, v29, v36
	v_add_f32_e32 v36, v30, v36
	v_add_f32_e32 v36, v31, v36
	v_add_f32_e32 v36, v32, v36
	v_add_f32_e32 v36, v33, v36
	v_add_f32_e32 v36, v34, v36
	v_add_f32_e32 v36, v35, v36
	s_nop 1
	v_mov_b32_dpp v37, v36 quad_perm:[1,0,3,2] row_mask:0xf bank_mask:0xf
	s_waitcnt lgkmcnt(0)
; __device__ __forceinline__ unsigned pk2(float lo, float hi) { f32x2_m v = {lo, hi}; bf16x2_m b = __builtin_convertvector(v, bf16x2_m); return __builtin_bit_cast(unsigned, b); }
; __device__ __forceinline__ float sigmoid_f(float x) { return __builtin_amdgcn_rcpf(1.0f + __builtin_amdgcn_exp2f(-LOG2E * x)); }
; __device__ __forceinline__ float wave_sum(float v) {
; #pragma unroll
;     for (int o = 1; o < 64; o <<= 1) v += __shfl_xor(v, o);
;     return v;
; }
; __device__ __forceinline__ void convpre_phase(const Ctx& C, const bf16* Z, const float* dw_w, const float* dw_b, const float* ln_g, const float* ln_b, bf16* ZC) {
;     ...
;             for (int q = 0; q < 4; ++q) {
;                 float s = 0.f;
; #pragma unroll
;                 for (int i = 0; i < 8; ++i) s += acc[q][i];
;                 const float mean = wave_sum(s) * (1.0f / CONV_CH); float s2 = 0.f;
; #pragma unroll
;                 for (int i = 0; i < 8; ++i) { acc[q][i] -= mean; s2 += acc[q][i] * acc[q][i]; }
;                 const float rstd = 1.0f / sqrtf(wave_sum(s2) * (1.0f / CONV_CH) + LN_EPS);
;                 float y[8];
; #pragma unroll
;                 for (int i = 0; i < 8; ++i) { const float u = acc[q][i] * rstd * lg[i] + lb[i]; y[i] = u * sigmoid_f(u); }
;                 v4u o; o.x = pk2(y[0], y[1]); o.y = pk2(y[2], y[3]); o.z = pk2(y[4], y[5]); o.w = pk2(y[6], y[7]);
;                 __builtin_amdgcn_raw_buffer_store_b128(o, zrs, (int)(((size_t)(t0 + tt + q) * CONV_CH + c0) * 2), 0, 16); }
	v_add_f32_e32 v36, v36, v37
	s_nop 1
	v_mov_b32_dpp v37, v36 quad_perm:[2,3,0,1] row_mask:0xf bank_mask:0xf
	s_waitcnt lgkmcnt(0)
	v_add_f32_e32 v36, v36, v37
	s_nop 1
	v_mov_b32_dpp v37, v36 row_half_mirror row_mask:0xf bank_mask:0xf
	s_waitcnt lgkmcnt(0)
	v_add_f32_e32 v36, v36, v37
	s_nop 1
	v_mov_b32_dpp v37, v36 row_mirror row_mask:0xf bank_mask:0xf
	s_waitcnt lgkmcnt(0)
	v_add_f32_e32 v36, v36, v37
	v_mov_b32_e32 v37, v36
	s_nop 1
	v_permlane16_swap_b32_e32 v36, v37
	s_waitcnt lgkmcnt(0)
	v_add_f32_e32 v36, v36, v37
	v_mov_b32_e32 v37, v36
	s_nop 1
	v_permlane32_swap_b32_e32 v36, v37
	s_waitcnt lgkmcnt(0)
	v_add_f32_e32 v36, v36, v37
	v_mul_f32_e32 v36, 0x3b000000, v36
	v_pk_add_f32 v[28:29], v[28:29], v[36:37] op_sel_hi:[1,0] neg_lo:[0,1] neg_hi:[0,1]
	v_pk_add_f32 v[34:35], v[34:35], v[36:37] op_sel_hi:[1,0] neg_lo:[0,1] neg_hi:[0,1]
	v_pk_add_f32 v[32:33], v[32:33], v[36:37] op_sel_hi:[1,0] neg_lo:[0,1] neg_hi:[0,1]
	v_pk_add_f32 v[30:31], v[30:31], v[36:37] op_sel_hi:[1,0] neg_lo:[0,1] neg_hi:[0,1]
	v_pk_mul_f32 v[36:37], v[28:29], v[28:29]
	v_pk_mul_f32 v[42:43], v[30:31], v[30:31]
	v_add_f32_e32 v36, v36, v37
	v_add_f32_e32 v36, v42, v36
	v_pk_mul_f32 v[40:41], v[32:33], v[32:33]
	v_add_f32_e32 v36, v43, v36
	v_add_f32_e32 v36, v40, v36
	v_pk_mul_f32 v[38:39], v[34:35], v[34:35]
	v_add_f32_e32 v36, v41, v36
	v_add_f32_e32 v36, v38, v36
	v_add_f32_e32 v36, v39, v36
	s_nop 1
	v_mov_b32_dpp v37, v36 quad_perm:[1,0,3,2] row_mask:0xf bank_mask:0xf
	s_waitcnt lgkmcnt(0)
	v_add_f32_e32 v36, v36, v37
	s_nop 1
	v_mov_b32_dpp v37, v36 quad_perm:[2,3,0,1] row_mask:0xf bank_mask:0xf
	s_waitcnt lgkmcnt(0)
	v_add_f32_e32 v36, v36, v37
	s_nop 1
	v_mov_b32_dpp v37, v36 row_half_mirror row_mask:0xf bank_mask:0xf
	s_waitcnt lgkmcnt(0)
	v_add_f32_e32 v36, v36, v37
	s_nop 1
	v_mov_b32_dpp v37, v36 row_mirror row_mask:0xf bank_mask:0xf
	s_waitcnt lgkmcnt(0)
	v_add_f32_e32 v36, v36, v37
	v_mov_b32_e32 v37, v36
	s_nop 1
	v_permlane16_swap_b32_e32 v36, v37
	s_waitcnt lgkmcnt(0)
	v_add_f32_e32 v36, v36, v37
	v_mov_b32_e32 v37, v36
	s_nop 1
	v_permlane32_swap_b32_e32 v36, v37
	s_waitcnt lgkmcnt(0)
	v_add_f32_e32 v36, v36, v37
	v_fmamk_f32 v36, v36, 0x3b000000, v210
	v_cmp_gt_f32_e32 vcc, s22, v36
	v_mul_f32_e32 v37, 0x4f800000, v36
	s_nop 0
	v_cndmask_b32_e32 v36, v36, v37, vcc
	v_sqrt_f32_e32 v37, v36
	s_nop 0
	v_add_u32_e32 v38, -1, v37
	v_fma_f32 v39, -v38, v37, v36
	v_cmp_ge_f32_e64 s[18:19], 0, v39
	v_add_u32_e32 v39, 1, v37
	s_nop 0
	v_cndmask_b32_e64 v38, v37, v38, s[18:19]
	v_fma_f32 v37, -v39, v37, v36
	v_cmp_lt_f32_e64 s[18:19], 0, v37
	s_nop 1
	v_cndmask_b32_e64 v37, v38, v39, s[18:19]
	v_mul_f32_e32 v38, 0x37800000, v37
	v_cndmask_b32_e32 v37, v37, v38, vcc
	v_cmp_class_f32_e32 vcc, v36, v211
	s_nop 1
	v_cndmask_b32_e32 v36, v37, v36, vcc
	v_div_scale_f32 v37, s[18:19], v36, v36, 1.0
	v_rcp_f32_e32 v38, v37
	s_nop 0
	v_fma_f32 v39, -v37, v38, 1.0
	v_fmac_f32_e32 v38, v39, v38
	v_div_scale_f32 v39, vcc, 1.0, v36, 1.0
	v_mul_f32_e32 v40, v39, v38
	v_fma_f32 v41, -v37, v40, v39
	v_fmac_f32_e32 v40, v41, v38
	v_fma_f32 v37, -v37, v40, v39
	v_div_fmas_f32 v37, v37, v38, v40
	v_div_fixup_f32 v36, v37, v36, 1.0
	v_pk_mul_f32 v[28:29], v[28:29], v[36:37] op_sel_hi:[1,0]
	s_nop 0
	v_pk_fma_f32 v[28:29], v[16:17], v[28:29], v[24:25]
	s_nop 0
	v_mul_f32_e32 v37, 0xbfb8aa3b, v28
	v_exp_f32_e32 v37, v37
	s_nop 0
	v_add_f32_e32 v37, 1.0, v37
	v_rcp_f32_e32 v38, v37
	v_mul_f32_e32 v37, 0xbfb8aa3b, v29
	v_exp_f32_e32 v37, v37
	s_nop 0
	v_add_f32_e32 v37, 1.0, v37
	v_pk_mul_f32 v[30:31], v[30:31], v[36:37] op_sel_hi:[1,0]
	v_rcp_f32_e32 v39, v37
	v_pk_fma_f32 v[30:31], v[18:19], v[30:31], v[26:27]
	v_pk_mul_f32 v[28:29], v[28:29], v[38:39]
	v_mul_f32_e32 v37, 0xbfb8aa3b, v30
	v_exp_f32_e32 v37, v37
	v_cvt_pk_bf16_f32 v28, v28, v29
	v_add_f32_e32 v37, 1.0, v37
	v_rcp_f32_e32 v38, v37
	v_mul_f32_e32 v37, 0xbfb8aa3b, v31
	v_exp_f32_e32 v37, v37
	s_nop 0
	v_add_f32_e32 v37, 1.0, v37
	v_pk_mul_f32 v[32:33], v[32:33], v[36:37] op_sel_hi:[1,0]
	v_rcp_f32_e32 v39, v37
	v_pk_fma_f32 v[32:33], v[12:13], v[32:33], v[20:21]
	v_pk_mul_f32 v[30:31], v[30:31], v[38:39]
	v_mul_f32_e32 v37, 0xbfb8aa3b, v32
	v_exp_f32_e32 v37, v37
	v_cvt_pk_bf16_f32 v29, v30, v31
	v_add_f32_e32 v37, 1.0, v37
	v_rcp_f32_e32 v38, v37
	v_mul_f32_e32 v37, 0xbfb8aa3b, v33
	v_exp_f32_e32 v37, v37
	s_nop 0
	v_add_f32_e32 v37, 1.0, v37
	v_pk_mul_f32 v[34:35], v[34:35], v[36:37] op_sel_hi:[1,0]
	v_rcp_f32_e32 v39, v37
	v_pk_fma_f32 v[34:35], v[14:15], v[34:35], v[22:23]
	v_pk_mul_f32 v[32:33], v[32:33], v[38:39]
	v_mul_f32_e32 v36, 0xbfb8aa3b, v34
	v_mul_f32_e32 v37, 0xbfb8aa3b, v35
	v_exp_f32_e32 v36, v36
	v_exp_f32_e32 v37, v37
	v_cvt_pk_bf16_f32 v30, v32, v33
	v_add_u32_e32 v32, s0, v108
	v_add_f32_e32 v36, 1.0, v36
	v_add_f32_e32 v37, 1.0, v37
	v_rcp_f32_e32 v36, v36
	v_rcp_f32_e32 v37, v37
	s_add_i32 s0, s20, 0x100
	s_cmpk_gt_i32 s20, 0xff
	s_mov_b32 s20, s0
	v_pk_mul_f32 v[34:35], v[34:35], v[36:37]
	s_nop 0
	v_cvt_pk_bf16_f32 v31, v34, v35
	buffer_store_dwordx4 v[28:31], v32, s[24:27], 0 offen sc1
	s_cbranch_scc1 .LBB0_514
